# v5 with the acquire-side L1 invalidate issued at barrier arrival instead of after release
# speedup vs baseline: 1.0376x; 1.0376x over previous
.LBB0_722:
	s_or_b64 exec, exec, s[6:7]
	v_readlane_b32 s6, v254, 19
	v_readlane_b32 s7, v254, 20
	s_waitcnt vmcnt(0)
	s_nop 3
	global_atomic_add v65, v167, s[6:7]
	s_waitcnt vmcnt(0)

.LBB0_781:
	v_readlane_b32 s6, v254, 17
	v_readlane_b32 s7, v254, 18
	v_cvt_f32_u32_e32 v1, v2
	v_sub_u32_e32 v4, 0, v2
	v_rcp_iflag_f32_e32 v1, v1
	s_nop 1
	buffer_inv sc1
	global_atomic_add v3, v65, v167, s[6:7] sc0
	v_mul_f32_e32 v1, 0x4f7ffffe, v1
	v_cvt_u32_f32_e32 v1, v1
	v_mul_lo_u32 v4, v4, v1
	v_mul_hi_u32 v4, v1, v4
	v_add_u32_e32 v1, v1, v4
	s_waitcnt vmcnt(0)
	v_mul_hi_u32 v1, v3, v1
	v_mul_lo_u32 v4, v1, v2
	v_sub_u32_e32 v4, v3, v4
	v_add_u32_e32 v5, 1, v1
	v_cmp_ge_u32_e32 vcc, v4, v2
	v_add_u32_e32 v3, 1, v3
	s_nop 0
	v_cndmask_b32_e32 v1, v1, v5, vcc
	v_sub_u32_e32 v5, v4, v2
	v_cndmask_b32_e32 v4, v4, v5, vcc
	v_add_u32_e32 v5, 1, v1
	v_cmp_ge_u32_e32 vcc, v4, v2
	s_nop 1
	v_cndmask_b32_e32 v1, v1, v5, vcc
	v_mul_lo_u32 v4, v2, v1
	v_add_u32_e32 v2, v4, v2
	v_cmp_ne_u32_e32 vcc, v3, v2
	s_and_saveexec_b64 s[6:7], vcc
	s_xor_b64 s[6:7], exec, s[6:7]
	s_cbranch_execz .LBB0_795
	v_readlane_b32 s8, v254, 19
	v_readlane_b32 s9, v254, 20
	s_waitcnt lgkmcnt(0)
	s_nop 3
	global_load_dword v0, v65, s[8:9] sc1
	s_waitcnt vmcnt(0)
	v_cmp_eq_u32_e32 vcc, v0, v1
	s_and_saveexec_b64 s[8:9], vcc
	s_cbranch_execz .LBB0_794
	s_mov_b32 s21, 1
	s_mov_b64 s[10:11], 0
	s_branch .LBB0_785

.LBB0_794:
	s_or_b64 exec, exec, s[8:9]
	s_waitcnt vmcnt(0)
	s_waitcnt vmcnt(0)

.LBB0_2518:
	v_readlane_b32 s6, v254, 17
	v_readlane_b32 s7, v254, 18
	v_cvt_f32_u32_e32 v1, v2
	v_sub_u32_e32 v4, 0, v2
	v_rcp_iflag_f32_e32 v1, v1
	s_nop 1
	buffer_inv sc1
	global_atomic_add v3, v65, v167, s[6:7] sc0
	v_mul_f32_e32 v1, 0x4f7ffffe, v1
	v_cvt_u32_f32_e32 v1, v1
	v_mul_lo_u32 v4, v4, v1
	v_mul_hi_u32 v4, v1, v4
	v_add_u32_e32 v1, v1, v4
	s_waitcnt vmcnt(0)
	v_mul_hi_u32 v1, v3, v1
	v_mul_lo_u32 v4, v1, v2
	v_sub_u32_e32 v4, v3, v4
	v_add_u32_e32 v5, 1, v1
	v_cmp_ge_u32_e32 vcc, v4, v2
	v_add_u32_e32 v3, 1, v3
	s_nop 0
	v_cndmask_b32_e32 v1, v1, v5, vcc
	v_sub_u32_e32 v5, v4, v2
	v_cndmask_b32_e32 v4, v4, v5, vcc
	v_add_u32_e32 v5, 1, v1
	v_cmp_ge_u32_e32 vcc, v4, v2
	s_nop 1
	v_cndmask_b32_e32 v1, v1, v5, vcc
	v_mul_lo_u32 v4, v2, v1
	v_add_u32_e32 v2, v4, v2
	v_cmp_ne_u32_e32 vcc, v3, v2
	s_and_saveexec_b64 s[6:7], vcc
	s_xor_b64 s[6:7], exec, s[6:7]
	s_cbranch_execz .LBB0_2532
	v_readlane_b32 s8, v254, 19
	v_readlane_b32 s9, v254, 20
	s_waitcnt lgkmcnt(0)
	s_nop 3
	global_load_dword v0, v65, s[8:9] sc1
	s_waitcnt vmcnt(0)
	v_cmp_eq_u32_e32 vcc, v0, v1
	s_and_saveexec_b64 s[8:9], vcc
	s_cbranch_execz .LBB0_2531
	s_mov_b32 s20, 1
	s_mov_b64 s[10:11], 0
	s_branch .LBB0_2522
